# grid barrier: XCD leaders add to the top counter without waiting for its return, every workgroup polls top >= (gen+1)*nx (no separate generation word)
# baseline (speedup 1.0000x reference)
; __device__ __forceinline__ unsigned xb_ld(unsigned* p)              { return __hip_atomic_load(p, __ATOMIC_RELAXED, __HIP_MEMORY_SCOPE_AGENT); }
; __device__ __forceinline__ unsigned xb_add(unsigned* p, unsigned v) { return __hip_atomic_fetch_add(p, v, __ATOMIC_RELAXED, __HIP_MEMORY_SCOPE_AGENT); }
; #define XB_SPIN(cond, bar) do { unsigned _sp = 0; while (cond) { __builtin_amdgcn_s_sleep(1); \
;     if ((++_sp & 255u) == 0u) { if (xb_ld(&(bar)[XB_TMO])) break; if (_sp > XB_SPIN_CAP) { atomicAdd(&(bar)[XB_TMO], 1u); break; } } } } while (0)
; template <class Idle>
; __device__ __forceinline__ void xcd_barrier(const XcdBarrier& b, Idle&& idle) {
;     ...
;         const unsigned old = xb_add(&bar[XB_XSUB(b.x)], 1u);
;         const unsigned gen = old / nloc;
;         if (old + 1u == (gen + 1u) * nloc) {
;             __builtin_amdgcn_fence(__ATOMIC_RELEASE, "agent");
;             asm volatile("s_waitcnt vmcnt(0)" ::: "memory");
;             const unsigned og = xb_add(&bar[XB_TOP], 1u);
;             const unsigned tg = og / nx;
;             if (og + 1u == (tg + 1u) * nx) xb_add(&bar[XB_TOPGEN], 1u);
;             else XB_SPIN(xb_ld(&bar[XB_TOPGEN]) == tg, bar);
;             __builtin_amdgcn_fence(__ATOMIC_ACQUIRE, "agent");
;             xb_add(&bar[XB_XGEN(b.x)], 1u);
;             asm volatile("s_waitcnt vmcnt(0)" ::: "memory");
;             b.st[2] = 1u;
;         } else { b.st[2] = 0u; b.st[3] = gen; }
.LBB0_75:
	s_andn2_saveexec_b64 s[6:7], s[6:7]
	s_cbranch_execz .LBB0_95
	s_mov_b64 s[6:7], exec
	buffer_wbl2 sc1
	s_waitcnt lgkmcnt(0)
	s_waitcnt vmcnt(0)
	v_mov_b32_e32 v5, 0x3000
	v_mov_b32_e32 v6, 1
	global_atomic_add v5, v6, s[74:75] offset:1024
	s_add_i32 s2, 0, 0x27ff8
	v_mov_b32_e32 v1, 0
	v_mov_b32_e32 v2, s2
	s_add_i32 s2, 0, 0x27ffc
	ds_write_b32 v2, v1
	v_mov_b32_e32 v1, s2
	ds_write_b32 v1, v3

; __device__ __forceinline__ unsigned xb_ld(unsigned* p)              { return __hip_atomic_load(p, __ATOMIC_RELAXED, __HIP_MEMORY_SCOPE_AGENT); }
; #define XB_SPIN(cond, bar) do { unsigned _sp = 0; while (cond) { __builtin_amdgcn_s_sleep(1); \
;     if ((++_sp & 255u) == 0u) { if (xb_ld(&(bar)[XB_TMO])) break; if (_sp > XB_SPIN_CAP) { atomicAdd(&(bar)[XB_TMO], 1u); break; } } } } while (0)
; template <class Idle>
; __device__ __forceinline__ void xcd_barrier(const XcdBarrier& b, Idle&& idle) {
;     ...
;         if (threadIdx.x == 0) {
;             unsigned* bar = b.bar; const unsigned gen = b.st[3];
;             bool rel = xb_ld(&bar[XB_XGEN(b.x)]) != gen;
;             if (!rel && anyw == 0ull) { XB_SPIN(xb_ld(&bar[XB_XGEN(b.x)]) == gen, bar); rel = true; }
.LBB0_116:
	s_lshl_b32 s0, s97, 8
	s_add_u32 s0, s74, s0
	s_addc_u32 s1, s75, 0
	s_add_u32 s0, s74, 0x3400
	s_addc_u32 s1, s75, 0
	s_add_i32 s12, 0, 0x27ffc
	v_mov_b32_e32 v1, 0
	v_mov_b32_e32 v2, 1
	v_mov_b32_e32 v3, s3
	s_branch .LBB0_120

; __device__ __forceinline__ unsigned xb_ld(unsigned* p)              { return __hip_atomic_load(p, __ATOMIC_RELAXED, __HIP_MEMORY_SCOPE_AGENT); }
; #define XB_SPIN(cond, bar) do { unsigned _sp = 0; while (cond) { __builtin_amdgcn_s_sleep(1); \
;     if ((++_sp & 255u) == 0u) { if (xb_ld(&(bar)[XB_TMO])) break; if (_sp > XB_SPIN_CAP) { atomicAdd(&(bar)[XB_TMO], 1u); break; } } } } while (0)
; template <class Idle>
; __device__ __forceinline__ void xcd_barrier(const XcdBarrier& b, Idle&& idle) {
;     ...
;         if (threadIdx.x == 0) {
;             unsigned* bar = b.bar; const unsigned gen = b.st[3];
;             bool rel = xb_ld(&bar[XB_XGEN(b.x)]) != gen;
;             if (!rel && anyw == 0ull) { XB_SPIN(xb_ld(&bar[XB_XGEN(b.x)]) == gen, bar); rel = true; }
.LBB0_120:
	s_barrier
	s_and_saveexec_b64 s[4:5], s[94:95]
	s_cbranch_execz .LBB0_119
	v_mov_b32_e32 v4, s12
	ds_read_b32 v4, v4
	global_load_dword v5, v1, s[0:1] sc1
	s_waitcnt vmcnt(0) lgkmcnt(0)
	v_mov_b32_e32 v6, 0x27ff4
	ds_read_b32 v6, v6
	s_waitcnt lgkmcnt(0)
	v_add_u32_e32 v4, 1, v4
	v_mul_lo_u32 v4, v4, v6
	v_cmp_ge_u32_e32 vcc, v5, v4
	s_cbranch_vccnz .LBB0_118
	global_load_dword v5, v1, s[0:1] sc1
	s_waitcnt vmcnt(0)
	v_cmp_ge_u32_e32 vcc, v5, v4
	s_cbranch_vccnz .LBB0_118
	s_mov_b32 s13, 1
	s_branch .LBB0_125

; __device__ __forceinline__ unsigned xb_ld(unsigned* p)              { return __hip_atomic_load(p, __ATOMIC_RELAXED, __HIP_MEMORY_SCOPE_AGENT); }
; #define XB_SPIN(cond, bar) do { unsigned _sp = 0; while (cond) { __builtin_amdgcn_s_sleep(1); \
;     if ((++_sp & 255u) == 0u) { if (xb_ld(&(bar)[XB_TMO])) break; if (_sp > XB_SPIN_CAP) { atomicAdd(&(bar)[XB_TMO], 1u); break; } } } } while (0)
; template <class Idle>
; __device__ __forceinline__ void xcd_barrier(const XcdBarrier& b, Idle&& idle) {
;     ...
;             if (!rel && anyw == 0ull) { XB_SPIN(xb_ld(&bar[XB_XGEN(b.x)]) == gen, bar); rel = true; }
.LBB0_127:
	global_load_dword v5, v1, s[0:1] sc1
	s_add_i32 s13, s13, 1
	s_mov_b64 s[8:9], -1
	s_waitcnt vmcnt(0)
	v_cmp_ge_u32_e64 s[6:7], v5, v4
	s_branch .LBB0_124

; __device__ __forceinline__ unsigned xb_ld(unsigned* p)              { return __hip_atomic_load(p, __ATOMIC_RELAXED, __HIP_MEMORY_SCOPE_AGENT); }
; __device__ __forceinline__ unsigned xb_add(unsigned* p, unsigned v) { return __hip_atomic_fetch_add(p, v, __ATOMIC_RELAXED, __HIP_MEMORY_SCOPE_AGENT); }
; #define XB_SPIN(cond, bar) do { unsigned _sp = 0; while (cond) { __builtin_amdgcn_s_sleep(1); \
;     if ((++_sp & 255u) == 0u) { if (xb_ld(&(bar)[XB_TMO])) break; if (_sp > XB_SPIN_CAP) { atomicAdd(&(bar)[XB_TMO], 1u); break; } } } } while (0)
; template <class Idle>
; __device__ __forceinline__ void xcd_barrier(const XcdBarrier& b, Idle&& idle) {
;     ...
;         const unsigned old = xb_add(&bar[XB_XSUB(b.x)], 1u);
;         const unsigned gen = old / nloc;
;         if (old + 1u == (gen + 1u) * nloc) {
;             __builtin_amdgcn_fence(__ATOMIC_RELEASE, "agent");
;             asm volatile("s_waitcnt vmcnt(0)" ::: "memory");
;             const unsigned og = xb_add(&bar[XB_TOP], 1u);
;             const unsigned tg = og / nx;
;             if (og + 1u == (tg + 1u) * nx) xb_add(&bar[XB_TOPGEN], 1u);
;             else XB_SPIN(xb_ld(&bar[XB_TOPGEN]) == tg, bar);
;             __builtin_amdgcn_fence(__ATOMIC_ACQUIRE, "agent");
;             xb_add(&bar[XB_XGEN(b.x)], 1u);
;             asm volatile("s_waitcnt vmcnt(0)" ::: "memory");
;             b.st[2] = 1u;
;         } else { b.st[2] = 0u; b.st[3] = gen; }
.LBB0_231:
	s_andn2_saveexec_b64 s[2:3], s[6:7]
	s_cbranch_execz .LBB0_251
	s_mov_b64 s[6:7], exec
	buffer_wbl2 sc1
	s_waitcnt lgkmcnt(0)
	s_waitcnt vmcnt(0)
	v_mov_b32_e32 v5, 0x3000
	v_mov_b32_e32 v6, 1
	global_atomic_add v5, v6, s[74:75] offset:1024
	s_add_i32 s2, 0, 0x27ff8
	v_mov_b32_e32 v1, 0
	v_mov_b32_e32 v2, s2
	s_add_i32 s2, 0, 0x27ffc
	ds_write_b32 v2, v1
	v_mov_b32_e32 v1, s2
	ds_write_b32 v1, v3

; __device__ __forceinline__ unsigned xb_ld(unsigned* p)              { return __hip_atomic_load(p, __ATOMIC_RELAXED, __HIP_MEMORY_SCOPE_AGENT); }
; __device__ __forceinline__ unsigned xb_add(unsigned* p, unsigned v) { return __hip_atomic_fetch_add(p, v, __ATOMIC_RELAXED, __HIP_MEMORY_SCOPE_AGENT); }
; #define XB_SPIN(cond, bar) do { unsigned _sp = 0; while (cond) { __builtin_amdgcn_s_sleep(1); \
;     if ((++_sp & 255u) == 0u) { if (xb_ld(&(bar)[XB_TMO])) break; if (_sp > XB_SPIN_CAP) { atomicAdd(&(bar)[XB_TMO], 1u); break; } } } } while (0)
; template <class Idle>
; __device__ __forceinline__ void xcd_barrier(const XcdBarrier& b, Idle&& idle) {
;     ...
;         const unsigned old = xb_add(&bar[XB_XSUB(b.x)], 1u);
;         const unsigned gen = old / nloc;
;         if (old + 1u == (gen + 1u) * nloc) {
;             __builtin_amdgcn_fence(__ATOMIC_RELEASE, "agent");
;             asm volatile("s_waitcnt vmcnt(0)" ::: "memory");
;             const unsigned og = xb_add(&bar[XB_TOP], 1u);
;             const unsigned tg = og / nx;
;             if (og + 1u == (tg + 1u) * nx) xb_add(&bar[XB_TOPGEN], 1u);
;             else XB_SPIN(xb_ld(&bar[XB_TOPGEN]) == tg, bar);
;             __builtin_amdgcn_fence(__ATOMIC_ACQUIRE, "agent");
;             xb_add(&bar[XB_XGEN(b.x)], 1u);
;             asm volatile("s_waitcnt vmcnt(0)" ::: "memory");
;             b.st[2] = 1u;
;         } else { b.st[2] = 0u; b.st[3] = gen; }
.LBB0_912:
	s_andn2_saveexec_b64 s[2:3], s[8:9]
	s_cbranch_execz .LBB0_932
	s_mov_b64 s[8:9], exec
	buffer_wbl2 sc1
	s_waitcnt lgkmcnt(0)
	s_waitcnt vmcnt(0)
	v_mov_b32_e32 v5, 0x3000
	v_mov_b32_e32 v6, 1
	global_atomic_add v5, v6, s[74:75] offset:1024
	s_add_i32 s2, 0, 0x27ff8
	v_mov_b32_e32 v1, 0
	v_mov_b32_e32 v2, s2
	s_add_i32 s2, 0, 0x27ffc
	ds_write_b32 v2, v1
	v_mov_b32_e32 v1, s2
	ds_write_b32 v1, v3

; __device__ __forceinline__ unsigned xb_ld(unsigned* p)              { return __hip_atomic_load(p, __ATOMIC_RELAXED, __HIP_MEMORY_SCOPE_AGENT); }
; #define XB_SPIN(cond, bar) do { unsigned _sp = 0; while (cond) { __builtin_amdgcn_s_sleep(1); \
;     if ((++_sp & 255u) == 0u) { if (xb_ld(&(bar)[XB_TMO])) break; if (_sp > XB_SPIN_CAP) { atomicAdd(&(bar)[XB_TMO], 1u); break; } } } } while (0)
; template <class Idle>
; __device__ __forceinline__ void xcd_barrier(const XcdBarrier& b, Idle&& idle) {
;     ...
;     unsigned rounds = 0u;
;     while (b.st[2] == 0u) {
;         const bool had = idle();
;         const unsigned long long anyw = __ballot(had);
;         __syncthreads();
;         if (threadIdx.x == 0) {
;             unsigned* bar = b.bar; const unsigned gen = b.st[3];
;             bool rel = xb_ld(&bar[XB_XGEN(b.x)]) != gen;
;             if (!rel && anyw == 0ull) { XB_SPIN(xb_ld(&bar[XB_XGEN(b.x)]) == gen, bar); rel = true; }
.LBB0_986:
	s_lshl_b32 s0, s97, 8
	s_add_u32 s0, s74, s0
	s_addc_u32 s1, s75, 0
	s_add_u32 s0, s74, 0x3400
	s_addc_u32 s1, s75, 0
	s_add_i32 s14, 0, 0x27ffc
	v_mov_b32_e32 v1, 0
	v_mov_b32_e32 v2, 1
	v_mov_b32_e32 v3, s3
	s_branch .LBB0_990

; __device__ __forceinline__ unsigned xb_ld(unsigned* p)              { return __hip_atomic_load(p, __ATOMIC_RELAXED, __HIP_MEMORY_SCOPE_AGENT); }
; #define XB_SPIN(cond, bar) do { unsigned _sp = 0; while (cond) { __builtin_amdgcn_s_sleep(1); \
;     if ((++_sp & 255u) == 0u) { if (xb_ld(&(bar)[XB_TMO])) break; if (_sp > XB_SPIN_CAP) { atomicAdd(&(bar)[XB_TMO], 1u); break; } } } } while (0)
; template <class Idle>
; __device__ __forceinline__ void xcd_barrier(const XcdBarrier& b, Idle&& idle) {
;     ...
;     while (b.st[2] == 0u) {
;         const bool had = idle();
;         const unsigned long long anyw = __ballot(had);
;         __syncthreads();
;         if (threadIdx.x == 0) {
;             unsigned* bar = b.bar; const unsigned gen = b.st[3];
;             bool rel = xb_ld(&bar[XB_XGEN(b.x)]) != gen;
;             if (!rel && anyw == 0ull) { XB_SPIN(xb_ld(&bar[XB_XGEN(b.x)]) == gen, bar); rel = true; }
;             if (!rel && ++rounds > (1u << 16)) { atomicAdd(&bar[XB_TMO], 1u); rel = true; }
;             if (rel) { __builtin_amdgcn_fence(__ATOMIC_ACQUIRE, "agent"); asm volatile("s_waitcnt vmcnt(0)" ::: "memory"); b.st[2] = 1u; }
.LBB0_990:
	s_barrier
	s_and_saveexec_b64 s[4:5], s[94:95]
	s_cbranch_execz .LBB0_989
	v_mov_b32_e32 v4, s14
	ds_read_b32 v4, v4
	global_load_dword v5, v1, s[0:1] sc1
	s_waitcnt vmcnt(0) lgkmcnt(0)
	v_mov_b32_e32 v6, 0x27ff4
	ds_read_b32 v6, v6
	s_waitcnt lgkmcnt(0)
	v_add_u32_e32 v4, 1, v4
	v_mul_lo_u32 v4, v4, v6
	v_cmp_ge_u32_e32 vcc, v5, v4
	s_cbranch_vccnz .LBB0_988
	global_load_dword v5, v1, s[0:1] sc1
	s_waitcnt vmcnt(0)
	v_cmp_ge_u32_e32 vcc, v5, v4
	s_cbranch_vccnz .LBB0_988
	s_mov_b32 s15, 1
	s_branch .LBB0_995

; __device__ __forceinline__ unsigned xb_ld(unsigned* p)              { return __hip_atomic_load(p, __ATOMIC_RELAXED, __HIP_MEMORY_SCOPE_AGENT); }
; #define XB_SPIN(cond, bar) do { unsigned _sp = 0; while (cond) { __builtin_amdgcn_s_sleep(1); \
;     if ((++_sp & 255u) == 0u) { if (xb_ld(&(bar)[XB_TMO])) break; if (_sp > XB_SPIN_CAP) { atomicAdd(&(bar)[XB_TMO], 1u); break; } } } } while (0)
; template <class Idle>
; __device__ __forceinline__ void xcd_barrier(const XcdBarrier& b, Idle&& idle) {
;     ...
;             if (!rel && anyw == 0ull) { XB_SPIN(xb_ld(&bar[XB_XGEN(b.x)]) == gen, bar); rel = true; }
.LBB0_997:
	global_load_dword v5, v1, s[0:1] sc1
	s_add_i32 s15, s15, 1
	s_mov_b64 s[10:11], -1
	s_waitcnt vmcnt(0)
	v_cmp_ge_u32_e64 s[8:9], v5, v4
	s_branch .LBB0_994
